# late conversion (hand-written) in three windows by XCD mod 3: before the GEMMs / before the proj GEMM / after
# speedup vs baseline: 1.0055x; 1.0055x over previous
;     __device__ __forceinline__ const char* pb(const Unit& u) const { return (const char*)(Bt + ((size_t)u.pn * BM * ldb + (size_t)u.sub * b_sub)); }
; __global__ void __launch_bounds__(NTHR, 2) mk_fwd(Args args) {
;     ...
;         if (IN(pb + 0)) {
;             { pg8::Gemm gm{(const bf16*)F.H8, (const bf16*)F.W8g, D / 2, D / 2, D / 2, 0, 0, 0}; pg8::StaticOrder S; S.init(M, GW, F.G, (int)blockIdx.x);
;               pg8::EpiGate8 E{(unsigned char*)F.GATES, GW / 256, F.b_gate + (size_t)l * GW};
;               pg8::gemm_phase<pg8::EpiGate8, pg8::StaticOrder, true, true, true>(ring, gm, S, E, F.wave); }
;             if ((int)blockIdx.x >= 160) { pg8::Gemm gm{(const bf16*)F.H8, (const bf16*)(F.W8g + (size_t)GW * D), D / 2, D / 2, D / 2, 0, 0, 0}; pg8::StaticOrder S; S.init(M, 6 * 256, F.G - 160, (int)blockIdx.x - 160);
;               pg8::EpiBf16<3> E{F.PROJ + O_Q, INWP, nullptr};
;               pg8::gemm_phase<pg8::EpiBf16<3>, pg8::StaticOrder, true, true, true>(ring, gm, S, E, F.wave); }
;             { pg8::Gemm gm{F.Hb, F.Wcat1, D, D, D, 0, 0, 0}; pg8::StaticOrder S; S.init(M, INWP - 6 * 256, F.G, (int)blockIdx.x, 1, O_Q / 256, 6);
;               pg8::EpiBf16<0> E{F.PROJ, INWP, nullptr};
;               pg8::gemm_phase<pg8::EpiBf16<0>, pg8::StaticOrder, true, true>(ring, gm, S, E, F.wave); }
;             {
;                 if ((int)blockIdx.x >= 160) { pg8::Gemm gf{F.Wbrx, F.Wpool, 1024, 256, 256, 256, 0, 0}; pg8::StaticOrder Sf; Sf.init(D, 1024, F.G, (int)blockIdx.x - 160);
;                     pg8::EpiBf16<0> Ef{F.Wbr, 1024, nullptr};
;                     pg8::gemm_phase<pg8::EpiBf16<0>, pg8::StaticOrder, true, true>(ring, gf, Sf, Ef, F.wave); }
;                 convert_weights<1>(F, l, 0);
.LBB0_99:
	s_mul_i32 s0, s6, 7
	v_writelane_b32 v255, s0, 42
	s_add_i32 s4, s0, 1
	v_readlane_b32 s0, v251, 14
	v_readlane_b32 s1, v251, 15
	s_cmp_le_i32 s0, s4
	s_cselect_b64 s[2:3], -1, 0
	s_cmp_lt_i32 s4, s1
	s_cselect_b64 s[4:5], -1, 0
	s_mov_b32 s7, s63
	s_and_b64 s[2:3], s[2:3], s[4:5]
	v_writelane_b32 v255, s6, 43
	s_andn2_b64 vcc, exec, s[2:3]
	s_nop 0
	v_writelane_b32 v255, s7, 44
	s_cbranch_vccnz .LBB0_239
	v_readlane_b32 s0, v255, 12
	s_mov_b32 s100, 0
	s_and_b32 s0, s0, 7
	s_mul_i32 s1, s0, 0x56
	s_lshr_b32 s1, s1, 8
	s_mul_i32 s1, s1, 3
	s_sub_u32 s0, s0, s1
	s_cmp_lt_u32 s0, 2
	s_cbranch_scc0 .Lp1_gemm_start
	s_mov_b32 s100, 3
	s_cmp_lt_u32 s0, 1
	s_cbranch_scc0 .Lp1_gemm_start
	s_mov_b32 s100, 1
	v_readlane_b32 s16, v255, 43
	v_readlane_b32 s17, v255, 44
	s_branch .LBB0_174

; __global__ void __launch_bounds__(NTHR, 2) mk_fwd(Args args) {
;     ...
;             { pg8::Gemm gm{F.Hb, F.Wcat1, D, D, D, 0, 0, 0}; pg8::StaticOrder S; S.init(M, INWP - 6 * 256, F.G, (int)blockIdx.x, 1, O_Q / 256, 6);
;               pg8::EpiBf16<0> E{F.PROJ, INWP, nullptr};
;               pg8::gemm_phase<pg8::EpiBf16<0>, pg8::StaticOrder, true, true>(ring, gm, S, E, F.wave); }
;     ...
;                 convert_weights<1>(F, l, 0);
.LBB0_133:
	s_cmp_eq_u32 s100, 3
	s_cbranch_scc0 .Lp1_mid_ret
	s_mov_b32 s100, 4
	s_mov_b32 s101, s19
	v_readlane_b32 s16, v255, 43
	v_readlane_b32 s17, v255, 44
	s_branch .LBB0_174

; __global__ void __launch_bounds__(NTHR, 2) mk_fwd(Args args) {
;     ...
;                 convert_weights<1>(F, l, 0);
.Lp1_chk_mid:
	s_cmp_eq_u32 s100, 4
	s_cbranch_scc0 .Lp1_conv_skip
	s_mov_b32 s100, 2
	s_mov_b32 s19, s101
	s_waitcnt lgkmcnt(0)
	s_barrier
	s_branch .Lp1_mid_ret
